# conv_experts load balance: workgroups 0..127 (busy with router GEMM + routing) hand 3 of their 16 tiles per 4096-tile weight job to workgroup w+128
# speedup vs baseline: 1.0122x; 1.0036x over previous
.LBB0_2820:
	s_add_i32 s43, s44, s93
	s_movk_i32 s32, 0xfff
	s_bitcmp0_b32 s92, 7
	s_cselect_b32 s32, 0xcff, s32
	s_cmp_gt_i32 s43, s32
	s_cbranch_scc0 .Lcbal0_go
	s_bitcmp1_b32 s44, 7
	s_cbranch_scc0 .Lcbal0_done
	s_add_i32 s43, s44, 0xfffffd80
	s_cmp_gt_i32 s43, 0xfff
	s_branch .Lcbal0_go
.Lcbal0_done:
	s_cmp_eq_u32 s92, s92
.Lcbal0_go:
	s_cselect_b64 s[26:27], -1, 0
	s_mov_b64 s[28:29], -1
	s_and_b64 vcc, exec, s[26:27]
	s_cbranch_vccz .LBB0_2822
	s_waitcnt vmcnt(0)
	s_lshl_b32 s45, s42, 16
	s_mov_b64 s[28:29], 0

.LBB0_2834:
	s_add_i32 s41, s42, s93
	s_movk_i32 s32, 0xfff
	s_bitcmp0_b32 s92, 7
	s_cselect_b32 s32, 0xcff, s32
	s_cmp_gt_i32 s41, s32
	s_cbranch_scc0 .Lcbal2_go
	s_bitcmp1_b32 s42, 7
	s_cbranch_scc0 .Lcbal2_done
	s_add_i32 s41, s42, 0xfffffd80
	s_cmp_gt_i32 s41, 0xfff
	s_branch .Lcbal2_go

.Lcbal2_go:
	s_cselect_b64 s[0:1], -1, 0
	s_mov_b64 s[26:27], -1
	s_and_b64 vcc, exec, s[0:1]
	s_cbranch_vccz .LBB0_2836
	s_waitcnt vmcnt(0)
	s_lshl_b32 s43, s40, 16
	s_mov_b64 s[26:27], 0

.LBB0_2859:
	s_nop 0
	s_nop 0
	s_nop 0
	s_nop 0
	s_nop 0
	s_nop 0
	s_nop 0
	s_nop 0
	s_nop 0
	s_waitcnt vmcnt(0)
	s_waitcnt vmcnt(0)
	s_barrier
	s_mov_b64 s[0:1], exec
	v_readlane_b32 s2, v253, 0
	v_readlane_b32 s3, v253, 1
	s_and_b64 s[2:3], s[0:1], s[2:3]
	s_mov_b64 exec, s[2:3]
	s_cbranch_execz .LBB0_2911
	s_add_i32 s2, 0, 0x27ff0
	v_mov_b32_e32 v1, s2
	s_waitcnt vmcnt(0) expcnt(0) lgkmcnt(0)
	ds_read_b32 v3, v1
	s_add_i32 s2, 0, 0x27ff4
	v_mov_b32_e32 v1, s2
	ds_read_b32 v1, v1
	s_waitcnt lgkmcnt(1)
	v_cmp_ne_u32_e32 vcc, 0, v3
	s_cbranch_vccnz .LBB0_2875
	v_readlane_b32 s2, v254, 0
	v_readlane_b32 s3, v254, 1
	s_load_dwordx2 s[4:5], s[2:3], 0x4
	s_add_u32 s2, s46, 0x1000
	s_addc_u32 s3, s47, 0
	s_add_u32 s6, s46, 0x1100
	s_addc_u32 s7, s47, 0
	s_add_u32 s8, s46, 0x1200
	s_addc_u32 s9, s47, 0
	s_waitcnt lgkmcnt(0)
	s_mul_i32 s4, s4, s93
	s_add_u32 s10, s46, 0x1300
	s_mul_i32 s4, s4, s5
	s_addc_u32 s11, s47, 0
	s_mov_b32 s5, 1
	v_mov_b32_e32 v17, 0
	s_branch .LBB0_2863
